# v3 attention loop plus static s_setprio 1 on waves 0-3 for the duration of the tile loop
# speedup vs baseline: 1.0088x; 1.0015x over previous
.LBB0_1088:
	v_lshlrev_b32_e32 v13, 3, v146
	v_and_b32_e32 v12, 0xc0, v12
	v_lshlrev_b32_e32 v14, 1, v146
	s_xor_b64 s[34:35], s[4:5], -1
	v_and_or_b32 v12, v13, 24, v12
	v_and_b32_e32 v14, 32, v14
	v_and_b32_e32 v13, 0x100, v13
	s_add_i32 s44, s44, s8
	v_or3_b32 v12, v12, v14, v13
	v_or_b32_e32 v13, s44, v145
	s_cmp_lg_u32 0, -1
	s_cselect_b32 s4, 0, 0
	s_lshr_b32 s46, s7, 6
	v_add_u32_e32 v163, 0xffffff91, v13
	v_lshlrev_b32_e32 v164, 4, v4
	v_lshlrev_b32_e32 v13, 4, v145
	s_add_i32 s38, 0, 0x10800
	s_add_i32 s47, s46, -2
	s_or_b32 s64, s44, 31
	v_and_b32_e32 v13, 0x70, v13
	v_add_u32_e32 v14, 32, v164
	v_lshl_add_u32 v171, v146, 2, s38
	s_lshl_b32 s38, s46, 8
	v_xad_u32 v168, v14, v13, 0
	v_add_u32_e32 v14, 64, v164
	s_add_u32 s38, s89, s38
	v_xad_u32 v169, v14, v13, 0
	v_add_u32_e32 v14, 0x60, v164
	s_addc_u32 s39, s88, 0
	s_and_b32 s7, s7, 0x1fc0
	s_add_i32 s6, s60, s6
	v_lshlrev_b32_e32 v144, 2, v4
	v_xad_u32 v166, v13, v164, 0
	v_xad_u32 v170, v14, v13, 0
	s_sub_i32 s65, s7, 64
	v_add_u32_e32 v13, s6, v145
	s_lshl_b32 s6, s46, 18
	v_ashrrev_i32_e32 v147, 31, v146
	v_sub_u32_e32 v13, v13, v144
	s_add_u32 s6, s90, s6
	v_lshl_add_u64 v[148:149], v[146:147], 2, s[38:39]
	v_subrev_u32_e32 v147, s7, v13
	s_addc_u32 s7, s91, 0
	v_add_u32_e32 v0, v0, v10
	v_lshl_add_u64 v[150:151], s[6:7], 0, v[0:1]
	v_add3_u32 v0, s61, v6, v11
	v_lshl_add_u64 v[152:153], s[6:7], 0, v[0:1]
	v_add_u32_e32 v0, v7, v5
	v_add3_u32 v0, v0, v8, v2
	v_lshl_or_b32 v0, v0, 12, v9
	v_add_u32_e32 v0, v0, v3
	v_lshl_add_u64 v[154:155], s[6:7], 0, v[0:1]
	v_add_u32_e32 v0, s62, v4
	v_lshlrev_b32_e32 v4, 1, v0
	s_mov_b32 s38, 0xffff0
	v_and_or_b32 v4, v4, s38, v5
	v_and_b32_e32 v0, 4, v0
	v_add_u32_e32 v162, s4, v12
	v_lshrrev_b32_e32 v12, 5, v146
	v_add_u32_e32 v0, v4, v0
	v_add_lshl_u32 v0, v0, v2, 12
	v_add_u16_e32 v2, 2, v12
	v_and_b32_e32 v2, 3, v2
	v_lshlrev_b32_e32 v2, 6, v2
	s_waitcnt vmcnt(0)
	v_or3_b32 v0, v0, v2, v3
	v_mov_b32_e32 v14, v1
	v_mov_b32_e32 v15, v1
	v_lshl_add_u64 v[156:157], s[6:7], 0, v[0:1]
	v_mov_b32_e32 v0, v1
	v_mov_b32_e32 v2, v1
	v_mov_b32_e32 v3, v1
	v_mov_b32_e32 v4, v1
	v_mov_b32_e32 v5, v1
	v_mov_b32_e32 v6, v1
	v_mov_b32_e32 v7, v1
	v_mov_b32_e32 v8, v1
	v_mov_b32_e32 v9, v1
	v_mov_b32_e32 v10, v1
	v_mov_b32_e32 v11, v1
	v_mov_b32_e32 v12, v1
	v_mov_b32_e32 v13, v1
	s_waitcnt lgkmcnt(0)
	v_mov_b64_e32 v[30:31], v[14:15]
	v_mov_b64_e32 v[46:47], v[14:15]
	v_mov_b64_e32 v[62:63], v[14:15]
	v_mov_b64_e32 v[78:79], v[14:15]
	s_mov_b32 s45, 0
	v_lshlrev_b32_e32 v165, 8, v145
	v_cmp_gt_u32_e64 s[4:5], 32, v146
	v_lshl_add_u32 v167, v145, 2, s54
	v_add_u32_e32 v161, s54, v164
	v_mov_b32_e32 v174, 0
	v_mov_b32_e32 v173, 0xf149f2ca
	s_mov_b32 s66, s46
	v_mov_b64_e32 v[28:29], v[12:13]
	v_mov_b64_e32 v[26:27], v[10:11]
	v_mov_b64_e32 v[24:25], v[8:9]
	v_mov_b64_e32 v[22:23], v[6:7]
	v_mov_b64_e32 v[20:21], v[4:5]
	v_mov_b64_e32 v[18:19], v[2:3]
	v_mov_b64_e32 v[16:17], v[0:1]
	v_mov_b64_e32 v[44:45], v[12:13]
	v_mov_b64_e32 v[42:43], v[10:11]
	v_mov_b64_e32 v[40:41], v[8:9]
	v_mov_b64_e32 v[38:39], v[6:7]
	v_mov_b64_e32 v[36:37], v[4:5]
	v_mov_b64_e32 v[34:35], v[2:3]
	v_mov_b64_e32 v[32:33], v[0:1]
	v_mov_b64_e32 v[60:61], v[12:13]
	v_mov_b64_e32 v[58:59], v[10:11]
	v_mov_b64_e32 v[56:57], v[8:9]
	v_mov_b64_e32 v[54:55], v[6:7]
	v_mov_b64_e32 v[52:53], v[4:5]
	v_mov_b64_e32 v[50:51], v[2:3]
	v_mov_b64_e32 v[48:49], v[0:1]
	v_mov_b64_e32 v[76:77], v[12:13]
	v_mov_b64_e32 v[74:75], v[10:11]
	v_mov_b64_e32 v[72:73], v[8:9]
	v_mov_b64_e32 v[70:71], v[6:7]
	v_mov_b64_e32 v[68:69], v[4:5]
	v_mov_b64_e32 v[66:67], v[2:3]
	v_mov_b64_e32 v[64:65], v[0:1]
	s_waitcnt vmcnt(0)
	s_barrier
	s_mov_b32 s45, 0
	s_lshl_b32 s65, s46, 6
	s_mov_b32 s66, 0
	s_mov_b32 s33, 0x8000
	s_mov_b32 s42, 0xc000
	s_mov_b32 s43, 0x11000
	s_mov_b32 s47, 0x10800
	s_mov_b32 s100, 0x10900
	s_mov_b32 s101, 0x10a00
	v_subrev_u32_e32 v147, 64, v147
	v_lshlrev_b32_e32 v232, 2, v146
	s_lshr_b32 s6, s68, 11
	s_and_b32 s7, s6, 3
	s_lshl_b32 s98, s7, 12
	s_lshl_b32 s99, s7, 16
	s_add_i32 s40, s46, -1
	s_lshl_b32 s41, s40, 8
	s_lshl_b32 s39, s40, 18
	s_add_u32 s40, s30, s41
	s_addc_u32 s41, s31, 0
	s_add_u32 s39, s39, s99
	s_cmp_ge_u32 s6, 4
	s_cbranch_scc1 .Lat_setup_b
	s_add_u32 s38, s82, s39
	s_addc_u32 s39, s83, 0
	v_lshrrev_b32_e32 v0, 4, v146
	v_and_b32_e32 v2, 15, v146
	v_xor_b32_e32 v2, v2, v0
	v_lshlrev_b32_e32 v2, 4, v2
	v_lshl_add_u32 v228, v0, 12, v2
	v_xor_b32_e32 v229, 64, v228
	v_add_u32_e32 v229, 0x4000, v229
	v_add_u32_e32 v230, 0x8000, v228
	v_xor_b32_e32 v231, 64, v228
	v_add_u32_e32 v231, 0xc000, v231
	s_add_i32 s6, s42, s98
	s_mov_b32 s7, s6
	s_mov_b32 m0, s7
	s_add_i32 s7, s7, 0x400
	global_load_lds_dwordx4 v228, s[38:39]
	s_mov_b32 m0, s7
	s_add_i32 s7, s7, 0x400
	global_load_lds_dwordx4 v229, s[38:39]
	s_mov_b32 m0, s7
	s_add_i32 s7, s7, 0x400
	global_load_lds_dwordx4 v230, s[38:39]
	s_mov_b32 m0, s7
	s_nop 0
	global_load_lds_dwordx4 v231, s[38:39]
	global_load_dword v154, v232, s[40:41]
	s_sub_u32 s38, s38, 0x40000
	s_subb_u32 s39, s39, 0
	s_sub_u32 s40, s40, 0x100
	s_subb_u32 s41, s41, 0
	s_setprio 1
	s_branch .Lat_setup_done

.Lat_done:
	s_setprio 0
